# grid barriers: acquire-side cache invalidate issued at arrival (the workgroup loads nothing between its arrival and the release) instead of after the release
# speedup vs baseline: 1.0130x; 1.0096x over previous
; __device__ __forceinline__ unsigned xb_ld(unsigned* p)              { return __hip_atomic_load(p, __ATOMIC_RELAXED, __HIP_MEMORY_SCOPE_AGENT); }
; __device__ __forceinline__ unsigned xb_add(unsigned* p, unsigned v) { return __hip_atomic_fetch_add(p, v, __ATOMIC_RELAXED, __HIP_MEMORY_SCOPE_AGENT); }
; __device__ __forceinline__ void xcd_barrier_complete(unsigned* bar, unsigned x, unsigned& nloc, unsigned& nx) {
;     const unsigned G = gridDim.x * gridDim.y * gridDim.z;
;     unsigned sum, cnt, mine, sp = 0u;
;     for (;;) {
;         sum = 0u; cnt = 0u; mine = 0u;
; #pragma unroll
;         for (unsigned j = 0; j < 16; ++j) { const unsigned c = xb_ld(&bar[XB_XCNT(j)]); sum += c; cnt += (c > 0u) ? 1u : 0u; mine = (j == x) ? c : mine; }
; __device__ __forceinline__ void xcd_barrier(const XcdBarrier& b) {
;     asm volatile("s_waitcnt vmcnt(0)" ::: "memory");
;     __syncthreads();
;     if (threadIdx.x == 0) {
;         unsigned* bar = b.bar;
;         __builtin_amdgcn_s_waitcnt(0);
;         unsigned nloc = b.st[0], nx = b.st[1];
;         if (nloc == 0u) { xcd_barrier_complete(bar, b.x, nloc, nx); b.st[0] = nloc; b.st[1] = nx; }
;         const unsigned old = xb_add(&bar[XB_XSUB(b.x)], 1u);
.LBB0_298:
	v_readlane_b32 s0, v255, 10
	v_readlane_b32 s1, v255, 11
	s_cmp_gt_i32 s1, 1
	s_cselect_b64 s[0:1], -1, 0
	s_and_b64 s[0:1], s[6:7], s[0:1]
	s_andn2_b64 vcc, exec, s[0:1]
	s_cbranch_vccnz .LBB0_352
	s_mov_b64 s[2:3], 0
	v_readlane_b32 s0, v255, 7
	s_waitcnt vmcnt(0)
	s_barrier
	s_nop 0
	v_writelane_b32 v255, s0, 7
	s_mov_b64 s[0:1], exec
	v_readlane_b32 s4, v255, 8
	v_readlane_b32 s5, v255, 9
	s_and_b64 s[4:5], s[0:1], s[4:5]
	s_mov_b64 exec, s[4:5]
	s_cbranch_execz .LBB0_351
	v_readlane_b32 s4, v255, 3
	v_readlane_b32 s6, v255, 5
	v_readlane_b32 s7, v255, 6
	s_add_u32 s2, s6, s2
	s_addc_u32 s3, s7, s3
	s_add_i32 s4, 0, 0x20160
	v_mov_b32_e32 v0, s4
	s_waitcnt vmcnt(0) expcnt(0) lgkmcnt(0)
	buffer_inv sc0 sc1
	ds_read_b32 v3, v0
	s_add_i32 s4, 0, 0x20164
	v_mov_b32_e32 v0, s4
	ds_read_b32 v1, v0
	v_readlane_b32 s5, v255, 4
	s_waitcnt lgkmcnt(1)
	v_cmp_ne_u32_e32 vcc, 0, v3
	s_cbranch_vccnz .LBB0_315
	v_readlane_b32 s4, v255, 0
	v_readlane_b32 s5, v255, 1
	s_load_dwordx2 s[8:9], s[4:5], 0x4
	s_add_u32 s4, s2, 0x4200
	s_addc_u32 s5, s3, 0
	s_add_u32 s6, s2, 0x4400
	s_addc_u32 s7, s3, 0
	v_readlane_b32 s10, v255, 2
	s_waitcnt lgkmcnt(0)
	s_mul_i32 s33, s8, s10
	s_add_u32 s8, s2, 0x4500
	s_mul_i32 s33, s33, s9
	s_addc_u32 s9, s3, 0
	s_add_u32 s10, s2, 0x4600
	s_addc_u32 s11, s3, 0
	s_add_u32 s12, s2, 0x4700
	s_addc_u32 s13, s3, 0
	s_add_u32 s14, s2, 0x4800
	s_addc_u32 s15, s3, 0
	s_add_u32 s16, s2, 0x4900
	s_addc_u32 s17, s3, 0
	s_add_u32 s18, s2, 0x4a00
	s_addc_u32 s19, s3, 0
	s_add_u32 s20, s2, 0x4b00
	s_addc_u32 s21, s3, 0
	s_add_u32 s22, s2, 0x4c00
	s_addc_u32 s23, s3, 0
	s_add_u32 s24, s2, 0x4d00
	s_addc_u32 s25, s3, 0
	s_add_u32 s26, s2, 0x4e00
	s_addc_u32 s27, s3, 0
	s_add_u32 s28, s2, 0x4f00
	s_addc_u32 s29, s3, 0
	s_add_u32 s30, s2, 0x5000
	s_addc_u32 s31, s3, 0
	s_add_u32 s34, s2, 0x5100
	s_addc_u32 s35, s3, 0
	s_add_u32 s36, s2, 0x5200
	s_addc_u32 s37, s3, 0
	s_add_u32 s38, s2, 0x5300
	s_addc_u32 s39, s3, 0
	s_mov_b32 s46, 1
	v_mov_b32_e32 v17, 0
	s_branch .LBB0_303

; __device__ __forceinline__ unsigned xb_ld(unsigned* p)              { return __hip_atomic_load(p, __ATOMIC_RELAXED, __HIP_MEMORY_SCOPE_AGENT); }
; #define XB_SPIN(cond, bar) do { unsigned _sp = 0; while (cond) { __builtin_amdgcn_s_sleep(1); \
;     if ((++_sp & 255u) == 0u) { if (xb_ld(&(bar)[XB_TMO])) break; if (_sp > XB_SPIN_CAP) { atomicAdd(&(bar)[XB_TMO], 1u); break; } } } } while (0)
; __device__ __forceinline__ void xcd_barrier(const XcdBarrier& b) {
;     ...
;             XB_SPIN(xb_ld(&bar[XB_XGEN(b.x)]) == gen, bar);
;             __builtin_amdgcn_fence(__ATOMIC_ACQUIRE, XB_SCOPE);
;             asm volatile("s_waitcnt vmcnt(0)" ::: "memory");
;         }
.LBB0_330:
	s_or_b64 exec, exec, s[6:7]
	s_waitcnt vmcnt(0)
	s_nop 0
	s_waitcnt vmcnt(0)

; __device__ __forceinline__ unsigned xb_ld(unsigned* p)              { return __hip_atomic_load(p, __ATOMIC_RELAXED, __HIP_MEMORY_SCOPE_AGENT); }
; __device__ __forceinline__ unsigned xb_add(unsigned* p, unsigned v) { return __hip_atomic_fetch_add(p, v, __ATOMIC_RELAXED, __HIP_MEMORY_SCOPE_AGENT); }
; #define XB_SPIN(cond, bar) do { unsigned _sp = 0; while (cond) { __builtin_amdgcn_s_sleep(1); \
;     if ((++_sp & 255u) == 0u) { if (xb_ld(&(bar)[XB_TMO])) break; if (_sp > XB_SPIN_CAP) { atomicAdd(&(bar)[XB_TMO], 1u); break; } } } } while (0)
; __device__ __forceinline__ void xcd_barrier(const XcdBarrier& b) {
;     ...
;             else XB_SPIN(xb_ld(&bar[XB_TOPGEN]) == tg, bar);
;             __builtin_amdgcn_fence(__ATOMIC_ACQUIRE, XB_SCOPE);
;             xb_add(&bar[XB_XGEN(b.x)], 1u);
;             asm volatile("s_waitcnt vmcnt(0)" ::: "memory");
.LBB0_348:
	s_or_b64 exec, exec, s[2:3]
	s_mov_b64 s[2:3], exec
	v_mbcnt_lo_u32_b32 v0, s2, 0
	v_mbcnt_hi_u32_b32 v0, s3, v0
	s_mov_b32 s7, 0
	v_cmp_eq_u32_e32 vcc, 0, v0
	s_waitcnt vmcnt(0)
	s_nop 0
	s_and_saveexec_b64 s[4:5], vcc
	s_cbranch_execz .LBB0_350
	s_add_i32 s6, s24, 0x900
	s_lshl_b64 s[6:7], s[6:7], 2
	s_add_u32 s6, s22, s6
	s_addc_u32 s7, s23, s7
	s_bcnt1_i32_b64 s2, s[2:3]
	v_mov_b32_e32 v0, 0
	v_mov_b32_e32 v1, s2
	global_atomic_add v0, v1, s[6:7]

; __device__ __forceinline__ unsigned xb_ld(unsigned* p)              { return __hip_atomic_load(p, __ATOMIC_RELAXED, __HIP_MEMORY_SCOPE_AGENT); }
; __device__ __forceinline__ unsigned xb_add(unsigned* p, unsigned v) { return __hip_atomic_fetch_add(p, v, __ATOMIC_RELAXED, __HIP_MEMORY_SCOPE_AGENT); }
; __device__ __forceinline__ void xcd_barrier_complete(unsigned* bar, unsigned x, unsigned& nloc, unsigned& nx) {
;     const unsigned G = gridDim.x * gridDim.y * gridDim.z;
;     unsigned sum, cnt, mine, sp = 0u;
;     for (;;) {
;         sum = 0u; cnt = 0u; mine = 0u;
; #pragma unroll
;         for (unsigned j = 0; j < 16; ++j) { const unsigned c = xb_ld(&bar[XB_XCNT(j)]); sum += c; cnt += (c > 0u) ? 1u : 0u; mine = (j == x) ? c : mine; }
; __device__ __forceinline__ void xcd_barrier(const XcdBarrier& b) {
;     asm volatile("s_waitcnt vmcnt(0)" ::: "memory");
;     __syncthreads();
;     if (threadIdx.x == 0) {
;         unsigned* bar = b.bar;
;         __builtin_amdgcn_s_waitcnt(0);
;         unsigned nloc = b.st[0], nx = b.st[1];
;         if (nloc == 0u) { xcd_barrier_complete(bar, b.x, nloc, nx); b.st[0] = nloc; b.st[1] = nx; }
;         const unsigned old = xb_add(&bar[XB_XSUB(b.x)], 1u);
.LBB0_394:
	v_readlane_b32 s2, v255, 14
	s_add_i32 s50, s2, 1
	v_readlane_b32 s2, v255, 10
	v_readlane_b32 s3, v255, 11
	s_cmp_lt_i32 s50, s3
	s_cselect_b64 s[2:3], -1, 0
	s_and_b64 s[0:1], s[0:1], s[2:3]
	s_andn2_b64 vcc, exec, s[0:1]
	s_cbranch_vccnz .LBB0_449
	s_mov_b64 s[4:5], 0
	v_readlane_b32 s0, v255, 7
	s_waitcnt vmcnt(0)
	s_barrier
	s_nop 0
	v_writelane_b32 v255, s0, 7
	s_mov_b64 s[0:1], exec
	v_readlane_b32 s6, v255, 8
	v_readlane_b32 s7, v255, 9
	s_and_b64 s[6:7], s[0:1], s[6:7]
	s_mov_b64 exec, s[6:7]
	s_cbranch_execz .LBB0_448
	v_readlane_b32 s6, v255, 15
	s_waitcnt vmcnt(0) expcnt(0) lgkmcnt(0)
	buffer_inv sc0 sc1
	v_readlane_b32 s8, v255, 3
	v_mov_b32_e32 v0, s6
	ds_read_b32 v4, v0
	v_readlane_b32 s6, v255, 16
	v_readlane_b32 s10, v255, 5
	v_readlane_b32 s11, v255, 6
	v_mov_b32_e32 v0, s6
	ds_read_b32 v2, v0
	s_add_u32 s4, s10, s4
	s_waitcnt lgkmcnt(1)
	v_cmp_ne_u32_e32 vcc, 0, v4
	s_addc_u32 s5, s11, s5
	v_readlane_b32 s9, v255, 4
	s_cbranch_vccnz .LBB0_412
	v_readlane_b32 s6, v255, 0
	v_readlane_b32 s7, v255, 1
	s_load_dwordx2 s[10:11], s[6:7], 0x4
	s_add_u32 s6, s4, 0x4200
	s_addc_u32 s7, s5, 0
	s_add_u32 s8, s4, 0x4400
	s_addc_u32 s9, s5, 0
	v_readlane_b32 s12, v255, 2
	s_waitcnt lgkmcnt(0)
	s_mul_i32 s51, s10, s12
	s_add_u32 s10, s4, 0x4500
	s_mul_i32 s51, s51, s11
	s_addc_u32 s11, s5, 0
	s_add_u32 s12, s4, 0x4600
	s_addc_u32 s13, s5, 0
	s_add_u32 s14, s4, 0x4700
	s_addc_u32 s15, s5, 0
	s_add_u32 s16, s4, 0x4800
	s_addc_u32 s17, s5, 0
	s_add_u32 s18, s4, 0x4900
	s_addc_u32 s19, s5, 0
	s_add_u32 s20, s4, 0x4a00
	s_addc_u32 s21, s5, 0
	s_add_u32 s22, s4, 0x4b00
	s_addc_u32 s23, s5, 0
	s_add_u32 s24, s4, 0x4c00
	s_addc_u32 s25, s5, 0
	s_add_u32 s26, s4, 0x4d00
	s_addc_u32 s27, s5, 0
	s_add_u32 s28, s4, 0x4e00
	s_addc_u32 s29, s5, 0
	s_add_u32 s30, s4, 0x4f00
	s_addc_u32 s31, s5, 0
	s_add_u32 s34, s4, 0x5000
	s_addc_u32 s35, s5, 0
	s_add_u32 s36, s4, 0x5100
	s_addc_u32 s37, s5, 0
	s_add_u32 s38, s4, 0x5200
	s_addc_u32 s39, s5, 0
	s_add_u32 s40, s4, 0x5300
	s_addc_u32 s41, s5, 0
	s_mov_b32 s52, 1
	s_branch .LBB0_399

; __device__ __forceinline__ unsigned xb_ld(unsigned* p)              { return __hip_atomic_load(p, __ATOMIC_RELAXED, __HIP_MEMORY_SCOPE_AGENT); }
; __device__ __forceinline__ unsigned xb_add(unsigned* p, unsigned v) { return __hip_atomic_fetch_add(p, v, __ATOMIC_RELAXED, __HIP_MEMORY_SCOPE_AGENT); }
; #define XB_SPIN(cond, bar) do { unsigned _sp = 0; while (cond) { __builtin_amdgcn_s_sleep(1); \
;     if ((++_sp & 255u) == 0u) { if (xb_ld(&(bar)[XB_TMO])) break; if (_sp > XB_SPIN_CAP) { atomicAdd(&(bar)[XB_TMO], 1u); break; } } } } while (0)
; __device__ __forceinline__ void xcd_barrier(const XcdBarrier& b) {
;     ...
;             __builtin_amdgcn_fence(__ATOMIC_ACQUIRE, XB_SCOPE);
;             xb_add(&bar[XB_XGEN(b.x)], 1u);
;             asm volatile("s_waitcnt vmcnt(0)" ::: "memory");
;         } else {
;             XB_SPIN(xb_ld(&bar[XB_XGEN(b.x)]) == gen, bar);
;             __builtin_amdgcn_fence(__ATOMIC_ACQUIRE, XB_SCOPE);
;             asm volatile("s_waitcnt vmcnt(0)" ::: "memory");
;         }
.LBB0_427:
	s_or_b64 exec, exec, s[8:9]
	s_waitcnt vmcnt(0) lgkmcnt(0)
	v_readlane_b32 s8, v255, 40
	s_nop 3
	s_cmp_eq_u32 s8, 1
	s_cbranch_scc1 .Lmy_nl_B1
	s_nop 0
	s_branch .Lmy_nl2_B1
.Lmy_nl_B1:
	s_nop 0
.Lmy_nl2_B1:
	s_waitcnt vmcnt(0)
.LBB0_428:
	s_andn2_saveexec_b64 s[6:7], s[6:7]
	s_cbranch_execz .LBB0_448
	v_readlane_b32 s8, v255, 40
	s_nop 3
	s_cmp_eq_u32 s8, 1
	s_cbranch_scc0 .Lmy_full_B1
	s_mov_b64 s[4:5], exec
	v_mbcnt_lo_u32_b32 v0, s4, 0
	v_mbcnt_hi_u32_b32 v0, s5, v0
	v_cmp_eq_u32_e32 vcc, 0, v0
	s_waitcnt vmcnt(0) lgkmcnt(0)
	s_nop 0
	s_branch .Lmy_xg_B1

; __device__ __forceinline__ unsigned xb_ld(unsigned* p)              { return __hip_atomic_load(p, __ATOMIC_RELAXED, __HIP_MEMORY_SCOPE_AGENT); }
; __device__ __forceinline__ unsigned xb_add(unsigned* p, unsigned v) { return __hip_atomic_fetch_add(p, v, __ATOMIC_RELAXED, __HIP_MEMORY_SCOPE_AGENT); }
; #define XB_SPIN(cond, bar) do { unsigned _sp = 0; while (cond) { __builtin_amdgcn_s_sleep(1); \
;     if ((++_sp & 255u) == 0u) { if (xb_ld(&(bar)[XB_TMO])) break; if (_sp > XB_SPIN_CAP) { atomicAdd(&(bar)[XB_TMO], 1u); break; } } } } while (0)
; __device__ __forceinline__ void xcd_barrier(const XcdBarrier& b) {
;     ...
;             else XB_SPIN(xb_ld(&bar[XB_TOPGEN]) == tg, bar);
;             __builtin_amdgcn_fence(__ATOMIC_ACQUIRE, XB_SCOPE);
;             xb_add(&bar[XB_XGEN(b.x)], 1u);
;             asm volatile("s_waitcnt vmcnt(0)" ::: "memory");
.LBB0_445:
	s_or_b64 exec, exec, s[4:5]
	s_mov_b64 s[4:5], exec
	v_mbcnt_lo_u32_b32 v0, s4, 0
	v_mbcnt_hi_u32_b32 v0, s5, v0
	v_cmp_eq_u32_e32 vcc, 0, v0
	s_waitcnt vmcnt(0)
	s_nop 0

; __device__ __forceinline__ unsigned xb_ld(unsigned* p)              { return __hip_atomic_load(p, __ATOMIC_RELAXED, __HIP_MEMORY_SCOPE_AGENT); }
; __device__ __forceinline__ unsigned xb_add(unsigned* p, unsigned v) { return __hip_atomic_fetch_add(p, v, __ATOMIC_RELAXED, __HIP_MEMORY_SCOPE_AGENT); }
; __device__ __forceinline__ void xcd_barrier_complete(unsigned* bar, unsigned x, unsigned& nloc, unsigned& nx) {
;     const unsigned G = gridDim.x * gridDim.y * gridDim.z;
;     unsigned sum, cnt, mine, sp = 0u;
;     for (;;) {
;         sum = 0u; cnt = 0u; mine = 0u;
; #pragma unroll
;         for (unsigned j = 0; j < 16; ++j) { const unsigned c = xb_ld(&bar[XB_XCNT(j)]); sum += c; cnt += (c > 0u) ? 1u : 0u; mine = (j == x) ? c : mine; }
; __device__ __forceinline__ void xcd_barrier(const XcdBarrier& b) {
;     asm volatile("s_waitcnt vmcnt(0)" ::: "memory");
;     __syncthreads();
;     if (threadIdx.x == 0) {
;         unsigned* bar = b.bar;
;         __builtin_amdgcn_s_waitcnt(0);
;         unsigned nloc = b.st[0], nx = b.st[1];
;         if (nloc == 0u) { xcd_barrier_complete(bar, b.x, nloc, nx); b.st[0] = nloc; b.st[1] = nx; }
;         const unsigned old = xb_add(&bar[XB_XSUB(b.x)], 1u);
.LBB0_777:
	v_readlane_b32 s2, v255, 14
	s_add_i32 s50, s2, 2
	v_readlane_b32 s2, v255, 10
	v_readlane_b32 s3, v255, 11
	s_cmp_lt_i32 s50, s3
	s_cselect_b64 s[2:3], -1, 0
	s_and_b64 s[0:1], s[0:1], s[2:3]
	s_andn2_b64 vcc, exec, s[0:1]
	s_cbranch_vccnz .LBB0_831
	s_mov_b64 s[4:5], 0
	v_readlane_b32 s0, v255, 7
	s_waitcnt vmcnt(0)
	s_waitcnt vmcnt(0)
	s_barrier
	v_writelane_b32 v255, s0, 7
	s_mov_b64 s[0:1], exec
	v_readlane_b32 s6, v255, 8
	v_readlane_b32 s7, v255, 9
	s_and_b64 s[6:7], s[0:1], s[6:7]
	s_mov_b64 exec, s[6:7]
	s_cbranch_execz .LBB0_830
	v_readlane_b32 s6, v255, 15
	s_waitcnt vmcnt(0) expcnt(0) lgkmcnt(0)
	buffer_inv sc0 sc1
	v_readlane_b32 s8, v255, 3
	v_mov_b32_e32 v0, s6
	ds_read_b32 v4, v0
	v_readlane_b32 s6, v255, 16
	v_readlane_b32 s10, v255, 5
	v_readlane_b32 s11, v255, 6
	v_mov_b32_e32 v0, s6
	ds_read_b32 v2, v0
	s_add_u32 s4, s10, s4
	s_waitcnt lgkmcnt(1)
	v_cmp_ne_u32_e32 vcc, 0, v4
	s_addc_u32 s5, s11, s5
	v_readlane_b32 s9, v255, 4
	s_cbranch_vccnz .LBB0_794
	v_readlane_b32 s6, v255, 0
	v_readlane_b32 s7, v255, 1
	s_load_dwordx2 s[10:11], s[6:7], 0x4
	s_add_u32 s6, s4, 0x4200
	s_addc_u32 s7, s5, 0
	s_add_u32 s8, s4, 0x4400
	s_addc_u32 s9, s5, 0
	v_readlane_b32 s12, v255, 2
	s_waitcnt lgkmcnt(0)
	s_mul_i32 s51, s10, s12
	s_add_u32 s10, s4, 0x4500
	s_mul_i32 s51, s51, s11
	s_addc_u32 s11, s5, 0
	s_add_u32 s12, s4, 0x4600
	s_addc_u32 s13, s5, 0
	s_add_u32 s14, s4, 0x4700
	s_addc_u32 s15, s5, 0
	s_add_u32 s16, s4, 0x4800
	s_addc_u32 s17, s5, 0
	s_add_u32 s18, s4, 0x4900
	s_addc_u32 s19, s5, 0
	s_add_u32 s20, s4, 0x4a00
	s_addc_u32 s21, s5, 0
	s_add_u32 s22, s4, 0x4b00
	s_addc_u32 s23, s5, 0
	s_add_u32 s24, s4, 0x4c00
	s_addc_u32 s25, s5, 0
	s_add_u32 s26, s4, 0x4d00
	s_addc_u32 s27, s5, 0
	s_add_u32 s28, s4, 0x4e00
	s_addc_u32 s29, s5, 0
	s_add_u32 s30, s4, 0x4f00
	s_addc_u32 s31, s5, 0
	s_add_u32 s34, s4, 0x5000
	s_addc_u32 s35, s5, 0
	s_add_u32 s36, s4, 0x5100
	s_addc_u32 s37, s5, 0
	s_add_u32 s38, s4, 0x5200
	s_addc_u32 s39, s5, 0
	s_add_u32 s40, s4, 0x5300
	s_addc_u32 s41, s5, 0
	s_mov_b32 s52, 1
	s_branch .LBB0_782

; __device__ __forceinline__ unsigned xb_ld(unsigned* p)              { return __hip_atomic_load(p, __ATOMIC_RELAXED, __HIP_MEMORY_SCOPE_AGENT); }
; #define XB_SPIN(cond, bar) do { unsigned _sp = 0; while (cond) { __builtin_amdgcn_s_sleep(1); \
;     if ((++_sp & 255u) == 0u) { if (xb_ld(&(bar)[XB_TMO])) break; if (_sp > XB_SPIN_CAP) { atomicAdd(&(bar)[XB_TMO], 1u); break; } } } } while (0)
; __device__ __forceinline__ void xcd_barrier(const XcdBarrier& b) {
;     ...
;             XB_SPIN(xb_ld(&bar[XB_XGEN(b.x)]) == gen, bar);
;             __builtin_amdgcn_fence(__ATOMIC_ACQUIRE, XB_SCOPE);
;             asm volatile("s_waitcnt vmcnt(0)" ::: "memory");
;         }
.LBB0_809:
	s_or_b64 exec, exec, s[8:9]
	s_waitcnt vmcnt(0) lgkmcnt(0)
	s_nop 0
	s_waitcnt vmcnt(0)

; __device__ __forceinline__ unsigned xb_ld(unsigned* p)              { return __hip_atomic_load(p, __ATOMIC_RELAXED, __HIP_MEMORY_SCOPE_AGENT); }
; __device__ __forceinline__ unsigned xb_add(unsigned* p, unsigned v) { return __hip_atomic_fetch_add(p, v, __ATOMIC_RELAXED, __HIP_MEMORY_SCOPE_AGENT); }
; #define XB_SPIN(cond, bar) do { unsigned _sp = 0; while (cond) { __builtin_amdgcn_s_sleep(1); \
;     if ((++_sp & 255u) == 0u) { if (xb_ld(&(bar)[XB_TMO])) break; if (_sp > XB_SPIN_CAP) { atomicAdd(&(bar)[XB_TMO], 1u); break; } } } } while (0)
; __device__ __forceinline__ void xcd_barrier(const XcdBarrier& b) {
;     ...
;             else XB_SPIN(xb_ld(&bar[XB_TOPGEN]) == tg, bar);
;             __builtin_amdgcn_fence(__ATOMIC_ACQUIRE, XB_SCOPE);
;             xb_add(&bar[XB_XGEN(b.x)], 1u);
;             asm volatile("s_waitcnt vmcnt(0)" ::: "memory");
.LBB0_827:
	s_or_b64 exec, exec, s[4:5]
	s_mov_b64 s[4:5], exec
	v_mbcnt_lo_u32_b32 v0, s4, 0
	v_mbcnt_hi_u32_b32 v0, s5, v0
	v_cmp_eq_u32_e32 vcc, 0, v0
	s_waitcnt vmcnt(0)
	s_nop 0
	s_and_saveexec_b64 s[6:7], vcc
	s_cbranch_execz .LBB0_829
	s_add_i32 s52, s26, 0x900
	s_lshl_b64 s[8:9], s[52:53], 2
	s_add_u32 s8, s24, s8
	s_addc_u32 s9, s25, s9
	s_bcnt1_i32_b64 s4, s[4:5]
	v_mov_b32_e32 v0, s4
	global_atomic_add v3, v0, s[8:9]

; __device__ __forceinline__ unsigned xb_ld(unsigned* p)              { return __hip_atomic_load(p, __ATOMIC_RELAXED, __HIP_MEMORY_SCOPE_AGENT); }
; __device__ __forceinline__ unsigned xb_add(unsigned* p, unsigned v) { return __hip_atomic_fetch_add(p, v, __ATOMIC_RELAXED, __HIP_MEMORY_SCOPE_AGENT); }
; __device__ __forceinline__ void xcd_barrier_complete(unsigned* bar, unsigned x, unsigned& nloc, unsigned& nx) {
;     const unsigned G = gridDim.x * gridDim.y * gridDim.z;
;     unsigned sum, cnt, mine, sp = 0u;
;     for (;;) {
;         sum = 0u; cnt = 0u; mine = 0u;
; #pragma unroll
;         for (unsigned j = 0; j < 16; ++j) { const unsigned c = xb_ld(&bar[XB_XCNT(j)]); sum += c; cnt += (c > 0u) ? 1u : 0u; mine = (j == x) ? c : mine; }
; __device__ __forceinline__ void xcd_barrier(const XcdBarrier& b) {
;     asm volatile("s_waitcnt vmcnt(0)" ::: "memory");
;     __syncthreads();
;     if (threadIdx.x == 0) {
;         unsigned* bar = b.bar;
;         __builtin_amdgcn_s_waitcnt(0);
;         unsigned nloc = b.st[0], nx = b.st[1];
;         if (nloc == 0u) { xcd_barrier_complete(bar, b.x, nloc, nx); b.st[0] = nloc; b.st[1] = nx; }
;         const unsigned old = xb_add(&bar[XB_XSUB(b.x)], 1u);
.LBB0_954:
	v_readlane_b32 s0, v255, 14
	s_add_i32 s50, s0, 3
	v_readlane_b32 s0, v255, 10
	v_readlane_b32 s1, v255, 11
	s_cmp_lt_i32 s50, s1
	s_cselect_b64 s[2:3], -1, 0
	s_and_b64 s[0:1], s[8:9], s[2:3]
	s_andn2_b64 vcc, exec, s[0:1]
	s_cbranch_vccnz .LBB0_1008
	s_mov_b64 s[4:5], 0
	v_readlane_b32 s0, v255, 7
	s_waitcnt vmcnt(0)
	s_waitcnt vmcnt(0) lgkmcnt(0)
	s_barrier
	v_writelane_b32 v255, s0, 7
	s_mov_b64 s[0:1], exec
	v_readlane_b32 s6, v255, 8
	v_readlane_b32 s7, v255, 9
	s_and_b64 s[6:7], s[0:1], s[6:7]
	s_mov_b64 exec, s[6:7]
	s_cbranch_execz .LBB0_1007
	v_readlane_b32 s6, v255, 15
	s_waitcnt vmcnt(0) expcnt(0) lgkmcnt(0)
	buffer_inv sc0 sc1
	v_readlane_b32 s8, v255, 3
	v_mov_b32_e32 v0, s6
	ds_read_b32 v4, v0
	v_readlane_b32 s6, v255, 16
	v_readlane_b32 s10, v255, 5
	v_readlane_b32 s11, v255, 6
	v_mov_b32_e32 v0, s6
	ds_read_b32 v2, v0
	s_add_u32 s4, s10, s4
	s_waitcnt lgkmcnt(1)
	v_cmp_ne_u32_e32 vcc, 0, v4
	s_addc_u32 s5, s11, s5
	v_readlane_b32 s9, v255, 4
	s_cbranch_vccnz .LBB0_971
	v_readlane_b32 s6, v255, 0
	v_readlane_b32 s7, v255, 1
	s_load_dwordx2 s[10:11], s[6:7], 0x4
	s_add_u32 s6, s4, 0x4200
	s_addc_u32 s7, s5, 0
	s_add_u32 s8, s4, 0x4400
	s_addc_u32 s9, s5, 0
	v_readlane_b32 s12, v255, 2
	s_waitcnt lgkmcnt(0)
	s_mul_i32 s51, s10, s12
	s_add_u32 s10, s4, 0x4500
	s_mul_i32 s51, s51, s11
	s_addc_u32 s11, s5, 0
	s_add_u32 s12, s4, 0x4600
	s_addc_u32 s13, s5, 0
	s_add_u32 s14, s4, 0x4700
	s_addc_u32 s15, s5, 0
	s_add_u32 s16, s4, 0x4800
	s_addc_u32 s17, s5, 0
	s_add_u32 s18, s4, 0x4900
	s_addc_u32 s19, s5, 0
	s_add_u32 s20, s4, 0x4a00
	s_addc_u32 s21, s5, 0
	s_add_u32 s22, s4, 0x4b00
	s_addc_u32 s23, s5, 0
	s_add_u32 s24, s4, 0x4c00
	s_addc_u32 s25, s5, 0
	s_add_u32 s26, s4, 0x4d00
	s_addc_u32 s27, s5, 0
	s_add_u32 s28, s4, 0x4e00
	s_addc_u32 s29, s5, 0
	s_add_u32 s30, s4, 0x4f00
	s_addc_u32 s31, s5, 0
	s_add_u32 s34, s4, 0x5000
	s_addc_u32 s35, s5, 0
	s_add_u32 s36, s4, 0x5100
	s_addc_u32 s37, s5, 0
	s_add_u32 s38, s4, 0x5200
	s_addc_u32 s39, s5, 0
	s_add_u32 s40, s4, 0x5300
	s_addc_u32 s41, s5, 0
	s_mov_b32 s52, 1
	s_branch .LBB0_959

; __global__ void __launch_bounds__(NWAVES * 64, 2) mega_fwd(Args args) {
;     ...
;             } else if (QMODE >= 3) {
;                 for (;;) {
;                     if (F.tid == 0) QS[0] = (int)__hip_atomic_fetch_add(F.ctl + CW_Q + 64 * F.l + 32, 1u, __ATOMIC_RELAXED, __HIP_MEMORY_SCOPE_AGENT);
;                     __syncthreads();
;                     const int j = __builtin_amdgcn_readfirstlane(QS[0]);
.LBB0_2845:
	s_mov_b64 s[26:27], exec
	v_cmp_eq_u32_e32 vcc, 0, v130
	s_and_b64 exec, exec, vcc
	s_cbranch_execz .Lmy_s4w_done
	s_add_u32 s0, s10, s12
	s_addc_u32 s1, s11, s13
	s_add_u32 s24, s0, 0x9080
	s_addc_u32 s25, s1, 0
	v_mov_b32_e32 v247, 1
	global_atomic_add v246, v3, v247, s[24:25] sc0
	s_add_u32 s28, s10, 0xb000
	s_addc_u32 s29, s11, 0
	s_add_i32 s30, s8, 1
	s_lshl_b32 s30, s30, 8
	s_mov_b32 s32, 0
	v_mov_b32_e32 v0, 0
	buffer_inv sc0 sc1

; __global__ void __launch_bounds__(NWAVES * 64, 2) mega_fwd(Args args) {
;     ...
;             } else if (QMODE >= 3) {
;                 for (;;) {
;                     if (F.tid == 0) QS[0] = (int)__hip_atomic_fetch_add(F.ctl + CW_Q + 64 * F.l + 32, 1u, __ATOMIC_RELAXED, __HIP_MEMORY_SCOPE_AGENT);
;                     __syncthreads();
;                     const int j = __builtin_amdgcn_readfirstlane(QS[0]);
.Lmy_s4w_ok:
	s_nop 0
	s_waitcnt vmcnt(0)

; __device__ __forceinline__ unsigned xb_ld(unsigned* p)              { return __hip_atomic_load(p, __ATOMIC_RELAXED, __HIP_MEMORY_SCOPE_AGENT); }
; __device__ __forceinline__ unsigned xb_add(unsigned* p, unsigned v) { return __hip_atomic_fetch_add(p, v, __ATOMIC_RELAXED, __HIP_MEMORY_SCOPE_AGENT); }
; __device__ __forceinline__ void xcd_barrier_complete(unsigned* bar, unsigned x, unsigned& nloc, unsigned& nx) {
;     const unsigned G = gridDim.x * gridDim.y * gridDim.z;
;     unsigned sum, cnt, mine, sp = 0u;
;     for (;;) {
;         sum = 0u; cnt = 0u; mine = 0u;
; #pragma unroll
;         for (unsigned j = 0; j < 16; ++j) { const unsigned c = xb_ld(&bar[XB_XCNT(j)]); sum += c; cnt += (c > 0u) ? 1u : 0u; mine = (j == x) ? c : mine; }
; __device__ __forceinline__ void xcd_barrier(const XcdBarrier& b) {
;     asm volatile("s_waitcnt vmcnt(0)" ::: "memory");
;     __syncthreads();
;     if (threadIdx.x == 0) {
;         unsigned* bar = b.bar;
;         __builtin_amdgcn_s_waitcnt(0);
;         unsigned nloc = b.st[0], nx = b.st[1];
;         if (nloc == 0u) { xcd_barrier_complete(bar, b.x, nloc, nx); b.st[0] = nloc; b.st[1] = nx; }
;         const unsigned old = xb_add(&bar[XB_XSUB(b.x)], 1u);
.LBB0_3096:
	v_readlane_b32 s0, v255, 14
	s_add_i32 s50, s0, 5
	v_readlane_b32 s0, v255, 10
	v_readlane_b32 s1, v255, 11
	s_cmp_lt_i32 s50, s1
	s_cselect_b64 s[2:3], -1, 0
	s_and_b64 s[0:1], s[14:15], s[2:3]
	s_andn2_b64 vcc, exec, s[0:1]
	s_cbranch_vccnz .LBB0_3150
	s_mov_b64 s[4:5], 0
	v_readlane_b32 s0, v255, 7
	s_waitcnt vmcnt(0)
	s_waitcnt vmcnt(0) lgkmcnt(0)
	s_barrier
	v_writelane_b32 v255, s0, 7
	s_mov_b64 s[0:1], exec
	v_readlane_b32 s6, v255, 8
	v_readlane_b32 s7, v255, 9
	s_and_b64 s[6:7], s[0:1], s[6:7]
	s_mov_b64 exec, s[6:7]
	s_cbranch_execz .LBB0_3149
	v_readlane_b32 s6, v255, 15
	s_waitcnt vmcnt(0) expcnt(0) lgkmcnt(0)
	buffer_inv sc0 sc1
	v_readlane_b32 s8, v255, 3
	v_mov_b32_e32 v0, s6
	ds_read_b32 v4, v0
	v_readlane_b32 s6, v255, 16
	v_readlane_b32 s10, v255, 5
	v_readlane_b32 s11, v255, 6
	v_mov_b32_e32 v0, s6
	ds_read_b32 v2, v0
	s_add_u32 s4, s10, s4
	s_waitcnt lgkmcnt(1)
	v_cmp_ne_u32_e32 vcc, 0, v4
	s_addc_u32 s5, s11, s5
	v_readlane_b32 s9, v255, 4
	s_cbranch_vccnz .LBB0_3113
	v_readlane_b32 s6, v255, 0
	v_readlane_b32 s7, v255, 1
	s_load_dwordx2 s[10:11], s[6:7], 0x4
	s_add_u32 s6, s4, 0x4200
	s_addc_u32 s7, s5, 0
	s_add_u32 s8, s4, 0x4400
	s_addc_u32 s9, s5, 0
	v_readlane_b32 s12, v255, 2
	s_waitcnt lgkmcnt(0)
	s_mul_i32 s51, s10, s12
	s_add_u32 s10, s4, 0x4500
	s_mul_i32 s51, s51, s11
	s_addc_u32 s11, s5, 0
	s_add_u32 s12, s4, 0x4600
	s_addc_u32 s13, s5, 0
	s_add_u32 s14, s4, 0x4700
	s_addc_u32 s15, s5, 0
	s_add_u32 s16, s4, 0x4800
	s_addc_u32 s17, s5, 0
	s_add_u32 s18, s4, 0x4900
	s_addc_u32 s19, s5, 0
	s_add_u32 s20, s4, 0x4a00
	s_addc_u32 s21, s5, 0
	s_add_u32 s22, s4, 0x4b00
	s_addc_u32 s23, s5, 0
	s_add_u32 s24, s4, 0x4c00
	s_addc_u32 s25, s5, 0
	s_add_u32 s26, s4, 0x4d00
	s_addc_u32 s27, s5, 0
	s_add_u32 s28, s4, 0x4e00
	s_addc_u32 s29, s5, 0
	s_add_u32 s30, s4, 0x4f00
	s_addc_u32 s31, s5, 0
	s_add_u32 s34, s4, 0x5000
	s_addc_u32 s35, s5, 0
	s_add_u32 s36, s4, 0x5100
	s_addc_u32 s37, s5, 0
	s_add_u32 s38, s4, 0x5200
	s_addc_u32 s39, s5, 0
	s_add_u32 s40, s4, 0x5300
	s_addc_u32 s41, s5, 0
	s_mov_b32 s52, 1
	s_branch .LBB0_3101

; __device__ __forceinline__ unsigned xb_ld(unsigned* p)              { return __hip_atomic_load(p, __ATOMIC_RELAXED, __HIP_MEMORY_SCOPE_AGENT); }
; __device__ __forceinline__ unsigned xb_add(unsigned* p, unsigned v) { return __hip_atomic_fetch_add(p, v, __ATOMIC_RELAXED, __HIP_MEMORY_SCOPE_AGENT); }
; __device__ __forceinline__ void xcd_barrier_complete(unsigned* bar, unsigned x, unsigned& nloc, unsigned& nx) {
;     const unsigned G = gridDim.x * gridDim.y * gridDim.z;
;     unsigned sum, cnt, mine, sp = 0u;
;     for (;;) {
;         sum = 0u; cnt = 0u; mine = 0u;
; #pragma unroll
;         for (unsigned j = 0; j < 16; ++j) { const unsigned c = xb_ld(&bar[XB_XCNT(j)]); sum += c; cnt += (c > 0u) ? 1u : 0u; mine = (j == x) ? c : mine; }
; __device__ __forceinline__ void xcd_barrier(const XcdBarrier& b) {
;     asm volatile("s_waitcnt vmcnt(0)" ::: "memory");
;     __syncthreads();
;     if (threadIdx.x == 0) {
;         unsigned* bar = b.bar;
;         __builtin_amdgcn_s_waitcnt(0);
;         unsigned nloc = b.st[0], nx = b.st[1];
;         if (nloc == 0u) { xcd_barrier_complete(bar, b.x, nloc, nx); b.st[0] = nloc; b.st[1] = nx; }
;         const unsigned old = xb_add(&bar[XB_XSUB(b.x)], 1u);
.LBB0_3175:
	v_readlane_b32 s2, v255, 14
	s_add_i32 s50, s2, 6
	v_readlane_b32 s2, v255, 10
	v_readlane_b32 s3, v255, 11
	s_cmp_lt_i32 s50, s3
	s_cselect_b64 s[2:3], -1, 0
	s_and_b64 s[0:1], s[0:1], s[2:3]
	s_andn2_b64 vcc, exec, s[0:1]
	s_cbranch_vccnz .LBB0_3229
	s_mov_b64 s[4:5], 0
	v_readlane_b32 s0, v255, 7
	s_waitcnt vmcnt(0)
	s_waitcnt vmcnt(0) lgkmcnt(0)
	s_barrier
	v_writelane_b32 v255, s0, 7
	s_mov_b64 s[0:1], exec
	v_readlane_b32 s6, v255, 8
	v_readlane_b32 s7, v255, 9
	s_and_b64 s[6:7], s[0:1], s[6:7]
	s_mov_b64 exec, s[6:7]
	s_cbranch_execz .LBB0_3228
	v_readlane_b32 s6, v255, 15
	s_waitcnt vmcnt(0) expcnt(0) lgkmcnt(0)
	buffer_inv sc0 sc1
	v_readlane_b32 s8, v255, 3
	v_mov_b32_e32 v0, s6
	ds_read_b32 v4, v0
	v_readlane_b32 s6, v255, 16
	v_readlane_b32 s10, v255, 5
	v_readlane_b32 s11, v255, 6
	v_mov_b32_e32 v0, s6
	ds_read_b32 v2, v0
	s_add_u32 s4, s10, s4
	s_waitcnt lgkmcnt(1)
	v_cmp_ne_u32_e32 vcc, 0, v4
	s_addc_u32 s5, s11, s5
	v_readlane_b32 s9, v255, 4
	s_cbranch_vccnz .LBB0_3192
	v_readlane_b32 s6, v255, 0
	v_readlane_b32 s7, v255, 1
	s_load_dwordx2 s[10:11], s[6:7], 0x4
	s_add_u32 s6, s4, 0x4200
	s_addc_u32 s7, s5, 0
	s_add_u32 s8, s4, 0x4400
	s_addc_u32 s9, s5, 0
	v_readlane_b32 s12, v255, 2
	s_waitcnt lgkmcnt(0)
	s_mul_i32 s51, s10, s12
	s_add_u32 s10, s4, 0x4500
	s_mul_i32 s51, s51, s11
	s_addc_u32 s11, s5, 0
	s_add_u32 s12, s4, 0x4600
	s_addc_u32 s13, s5, 0
	s_add_u32 s14, s4, 0x4700
	s_addc_u32 s15, s5, 0
	s_add_u32 s16, s4, 0x4800
	s_addc_u32 s17, s5, 0
	s_add_u32 s18, s4, 0x4900
	s_addc_u32 s19, s5, 0
	s_add_u32 s20, s4, 0x4a00
	s_addc_u32 s21, s5, 0
	s_add_u32 s22, s4, 0x4b00
	s_addc_u32 s23, s5, 0
	s_add_u32 s24, s4, 0x4c00
	s_addc_u32 s25, s5, 0
	s_add_u32 s26, s4, 0x4d00
	s_addc_u32 s27, s5, 0
	s_add_u32 s28, s4, 0x4e00
	s_addc_u32 s29, s5, 0
	s_add_u32 s30, s4, 0x4f00
	s_addc_u32 s31, s5, 0
	s_add_u32 s34, s4, 0x5000
	s_addc_u32 s35, s5, 0
	s_add_u32 s36, s4, 0x5100
	s_addc_u32 s37, s5, 0
	s_add_u32 s38, s4, 0x5200
	s_addc_u32 s39, s5, 0
	s_add_u32 s40, s4, 0x5300
	s_addc_u32 s41, s5, 0
	s_mov_b32 s52, 1
	s_branch .LBB0_3180

; __device__ __forceinline__ unsigned xb_ld(unsigned* p)              { return __hip_atomic_load(p, __ATOMIC_RELAXED, __HIP_MEMORY_SCOPE_AGENT); }
; #define XB_SPIN(cond, bar) do { unsigned _sp = 0; while (cond) { __builtin_amdgcn_s_sleep(1); \
;     if ((++_sp & 255u) == 0u) { if (xb_ld(&(bar)[XB_TMO])) break; if (_sp > XB_SPIN_CAP) { atomicAdd(&(bar)[XB_TMO], 1u); break; } } } } while (0)
; __device__ __forceinline__ void xcd_barrier(const XcdBarrier& b) {
;     ...
;             XB_SPIN(xb_ld(&bar[XB_XGEN(b.x)]) == gen, bar);
;             __builtin_amdgcn_fence(__ATOMIC_ACQUIRE, XB_SCOPE);
;             asm volatile("s_waitcnt vmcnt(0)" ::: "memory");
;         }
.Lmy_nl_B6:
	s_nop 0
.Lmy_nl2_B6:
	s_waitcnt vmcnt(0)

; __device__ __forceinline__ unsigned xb_ld(unsigned* p)              { return __hip_atomic_load(p, __ATOMIC_RELAXED, __HIP_MEMORY_SCOPE_AGENT); }
; __device__ __forceinline__ unsigned xb_add(unsigned* p, unsigned v) { return __hip_atomic_fetch_add(p, v, __ATOMIC_RELAXED, __HIP_MEMORY_SCOPE_AGENT); }
; __device__ __forceinline__ void xcd_barrier_complete(unsigned* bar, unsigned x, unsigned& nloc, unsigned& nx) {
;     const unsigned G = gridDim.x * gridDim.y * gridDim.z;
;     unsigned sum, cnt, mine, sp = 0u;
;     for (;;) {
;         sum = 0u; cnt = 0u; mine = 0u;
; #pragma unroll
;         for (unsigned j = 0; j < 16; ++j) { const unsigned c = xb_ld(&bar[XB_XCNT(j)]); sum += c; cnt += (c > 0u) ? 1u : 0u; mine = (j == x) ? c : mine; }
; __device__ __forceinline__ void xcd_barrier(const XcdBarrier& b) {
;     asm volatile("s_waitcnt vmcnt(0)" ::: "memory");
;     __syncthreads();
;     if (threadIdx.x == 0) {
;         unsigned* bar = b.bar;
;         __builtin_amdgcn_s_waitcnt(0);
;         unsigned nloc = b.st[0], nx = b.st[1];
;         if (nloc == 0u) { xcd_barrier_complete(bar, b.x, nloc, nx); b.st[0] = nloc; b.st[1] = nx; }
;         const unsigned old = xb_add(&bar[XB_XSUB(b.x)], 1u);
.LBB0_3378:
	v_readlane_b32 s0, v255, 14
	s_add_i32 s50, s0, 8
	v_readlane_b32 s0, v255, 10
	v_readlane_b32 s1, v255, 11
	s_cmp_lt_i32 s50, s1
	s_cselect_b64 s[0:1], -1, 0
	s_and_b64 s[2:3], s[12:13], s[0:1]
	s_andn2_b64 vcc, exec, s[2:3]
	s_cbranch_vccnz .LBB0_3432
	s_mov_b64 s[4:5], 0
	v_readlane_b32 s2, v255, 7
	s_waitcnt vmcnt(0)
	s_waitcnt vmcnt(0) lgkmcnt(0)
	s_barrier
	v_writelane_b32 v255, s2, 7
	s_mov_b64 s[2:3], exec
	v_readlane_b32 s6, v255, 8
	v_readlane_b32 s7, v255, 9
	s_and_b64 s[6:7], s[2:3], s[6:7]
	s_mov_b64 exec, s[6:7]
	s_cbranch_execz .LBB0_3431
	v_readlane_b32 s6, v255, 15
	s_waitcnt vmcnt(0) expcnt(0) lgkmcnt(0)
	buffer_inv sc0 sc1
	v_readlane_b32 s8, v255, 3
	v_mov_b32_e32 v0, s6
	ds_read_b32 v4, v0
	v_readlane_b32 s6, v255, 16
	v_readlane_b32 s10, v255, 5
	v_readlane_b32 s11, v255, 6
	v_mov_b32_e32 v0, s6
	ds_read_b32 v2, v0
	s_add_u32 s4, s10, s4
	s_waitcnt lgkmcnt(1)
	v_cmp_ne_u32_e32 vcc, 0, v4
	s_addc_u32 s5, s11, s5
	v_readlane_b32 s9, v255, 4
	s_cbranch_vccnz .LBB0_3395
	v_readlane_b32 s6, v255, 0
	v_readlane_b32 s7, v255, 1
	s_load_dwordx2 s[10:11], s[6:7], 0x4
	s_add_u32 s6, s4, 0x4200
	s_addc_u32 s7, s5, 0
	s_add_u32 s8, s4, 0x4400
	s_addc_u32 s9, s5, 0
	v_readlane_b32 s12, v255, 2
	s_waitcnt lgkmcnt(0)
	s_mul_i32 s51, s10, s12
	s_add_u32 s10, s4, 0x4500
	s_mul_i32 s51, s51, s11
	s_addc_u32 s11, s5, 0
	s_add_u32 s12, s4, 0x4600
	s_addc_u32 s13, s5, 0
	s_add_u32 s14, s4, 0x4700
	s_addc_u32 s15, s5, 0
	s_add_u32 s16, s4, 0x4800
	s_addc_u32 s17, s5, 0
	s_add_u32 s18, s4, 0x4900
	s_addc_u32 s19, s5, 0
	s_add_u32 s20, s4, 0x4a00
	s_addc_u32 s21, s5, 0
	s_add_u32 s22, s4, 0x4b00
	s_addc_u32 s23, s5, 0
	s_add_u32 s24, s4, 0x4c00
	s_addc_u32 s25, s5, 0
	s_add_u32 s26, s4, 0x4d00
	s_addc_u32 s27, s5, 0
	s_add_u32 s28, s4, 0x4e00
	s_addc_u32 s29, s5, 0
	s_add_u32 s30, s4, 0x4f00
	s_addc_u32 s31, s5, 0
	s_add_u32 s34, s4, 0x5000
	s_addc_u32 s35, s5, 0
	s_add_u32 s36, s4, 0x5100
	s_addc_u32 s37, s5, 0
	s_add_u32 s38, s4, 0x5200
	s_addc_u32 s39, s5, 0
	s_add_u32 s40, s4, 0x5300
	s_addc_u32 s41, s5, 0
	s_mov_b32 s52, 1
	s_branch .LBB0_3383

; __device__ __forceinline__ unsigned xb_ld(unsigned* p)              { return __hip_atomic_load(p, __ATOMIC_RELAXED, __HIP_MEMORY_SCOPE_AGENT); }
; __device__ __forceinline__ unsigned xb_add(unsigned* p, unsigned v) { return __hip_atomic_fetch_add(p, v, __ATOMIC_RELAXED, __HIP_MEMORY_SCOPE_AGENT); }
; __device__ __forceinline__ void xcd_barrier_complete(unsigned* bar, unsigned x, unsigned& nloc, unsigned& nx) {
;     const unsigned G = gridDim.x * gridDim.y * gridDim.z;
;     unsigned sum, cnt, mine, sp = 0u;
;     for (;;) {
;         sum = 0u; cnt = 0u; mine = 0u;
; #pragma unroll
;         for (unsigned j = 0; j < 16; ++j) { const unsigned c = xb_ld(&bar[XB_XCNT(j)]); sum += c; cnt += (c > 0u) ? 1u : 0u; mine = (j == x) ? c : mine; }
; __device__ __forceinline__ void xcd_barrier(const XcdBarrier& b) {
;     asm volatile("s_waitcnt vmcnt(0)" ::: "memory");
;     __syncthreads();
;     if (threadIdx.x == 0) {
;         unsigned* bar = b.bar;
;         __builtin_amdgcn_s_waitcnt(0);
;         unsigned nloc = b.st[0], nx = b.st[1];
;         if (nloc == 0u) { xcd_barrier_complete(bar, b.x, nloc, nx); b.st[0] = nloc; b.st[1] = nx; }
;         const unsigned old = xb_add(&bar[XB_XSUB(b.x)], 1u);
.LBB0_3452:
	v_readlane_b32 s0, v255, 14
	s_add_i32 s50, s0, 9
	v_readlane_b32 s0, v255, 10
	v_readlane_b32 s1, v255, 11
	s_cmp_lt_i32 s50, s1
	s_cselect_b64 s[0:1], -1, 0
	s_and_b64 s[2:3], s[12:13], s[0:1]
	s_andn2_b64 vcc, exec, s[2:3]
	s_cbranch_vccnz .LBB0_3506
	s_mov_b64 s[4:5], 0
	v_readlane_b32 s2, v255, 7
	s_waitcnt vmcnt(0)
	s_waitcnt vmcnt(0) lgkmcnt(0)
	s_barrier
	v_writelane_b32 v255, s2, 7
	s_mov_b64 s[2:3], exec
	v_readlane_b32 s6, v255, 8
	v_readlane_b32 s7, v255, 9
	s_and_b64 s[6:7], s[2:3], s[6:7]
	s_mov_b64 exec, s[6:7]
	s_cbranch_execz .LBB0_3505
	v_readlane_b32 s6, v255, 15
	s_waitcnt vmcnt(0) expcnt(0) lgkmcnt(0)
	buffer_inv sc0 sc1
	v_readlane_b32 s8, v255, 3
	v_mov_b32_e32 v0, s6
	ds_read_b32 v4, v0
	v_readlane_b32 s6, v255, 16
	v_readlane_b32 s10, v255, 5
	v_readlane_b32 s11, v255, 6
	v_mov_b32_e32 v0, s6
	ds_read_b32 v2, v0
	s_add_u32 s4, s10, s4
	s_waitcnt lgkmcnt(1)
	v_cmp_ne_u32_e32 vcc, 0, v4
	s_addc_u32 s5, s11, s5
	v_readlane_b32 s9, v255, 4
	s_cbranch_vccnz .LBB0_3469
	v_readlane_b32 s6, v255, 0
	v_readlane_b32 s7, v255, 1
	s_load_dwordx2 s[10:11], s[6:7], 0x4
	s_add_u32 s6, s4, 0x4200
	s_addc_u32 s7, s5, 0
	s_add_u32 s8, s4, 0x4400
	s_addc_u32 s9, s5, 0
	v_readlane_b32 s12, v255, 2
	s_waitcnt lgkmcnt(0)
	s_mul_i32 s51, s10, s12
	s_add_u32 s10, s4, 0x4500
	s_mul_i32 s51, s51, s11
	s_addc_u32 s11, s5, 0
	s_add_u32 s12, s4, 0x4600
	s_addc_u32 s13, s5, 0
	s_add_u32 s14, s4, 0x4700
	s_addc_u32 s15, s5, 0
	s_add_u32 s16, s4, 0x4800
	s_addc_u32 s17, s5, 0
	s_add_u32 s18, s4, 0x4900
	s_addc_u32 s19, s5, 0
	s_add_u32 s20, s4, 0x4a00
	s_addc_u32 s21, s5, 0
	s_add_u32 s22, s4, 0x4b00
	s_addc_u32 s23, s5, 0
	s_add_u32 s24, s4, 0x4c00
	s_addc_u32 s25, s5, 0
	s_add_u32 s26, s4, 0x4d00
	s_addc_u32 s27, s5, 0
	s_add_u32 s28, s4, 0x4e00
	s_addc_u32 s29, s5, 0
	s_add_u32 s30, s4, 0x4f00
	s_addc_u32 s31, s5, 0
	s_add_u32 s34, s4, 0x5000
	s_addc_u32 s35, s5, 0
	s_add_u32 s36, s4, 0x5100
	s_addc_u32 s37, s5, 0
	s_add_u32 s38, s4, 0x5200
	s_addc_u32 s39, s5, 0
	s_add_u32 s40, s4, 0x5300
	s_addc_u32 s41, s5, 0
	s_mov_b32 s52, 1
	s_branch .LBB0_3457

; __device__ __forceinline__ unsigned xb_ld(unsigned* p)              { return __hip_atomic_load(p, __ATOMIC_RELAXED, __HIP_MEMORY_SCOPE_AGENT); }
; __device__ __forceinline__ unsigned xb_add(unsigned* p, unsigned v) { return __hip_atomic_fetch_add(p, v, __ATOMIC_RELAXED, __HIP_MEMORY_SCOPE_AGENT); }
; __device__ __forceinline__ void xcd_barrier_complete(unsigned* bar, unsigned x, unsigned& nloc, unsigned& nx) {
;     const unsigned G = gridDim.x * gridDim.y * gridDim.z;
;     unsigned sum, cnt, mine, sp = 0u;
;     for (;;) {
;         sum = 0u; cnt = 0u; mine = 0u;
; #pragma unroll
;         for (unsigned j = 0; j < 16; ++j) { const unsigned c = xb_ld(&bar[XB_XCNT(j)]); sum += c; cnt += (c > 0u) ? 1u : 0u; mine = (j == x) ? c : mine; }
; __device__ __forceinline__ void xcd_barrier(const XcdBarrier& b) {
;     asm volatile("s_waitcnt vmcnt(0)" ::: "memory");
;     __syncthreads();
;     if (threadIdx.x == 0) {
;         unsigned* bar = b.bar;
;         __builtin_amdgcn_s_waitcnt(0);
;         unsigned nloc = b.st[0], nx = b.st[1];
;         if (nloc == 0u) { xcd_barrier_complete(bar, b.x, nloc, nx); b.st[0] = nloc; b.st[1] = nx; }
;         const unsigned old = xb_add(&bar[XB_XSUB(b.x)], 1u);
.LBB0_3803:
	v_readlane_b32 s0, v255, 14
	s_add_i32 s50, s0, 10
	v_readlane_b32 s0, v255, 10
	v_readlane_b32 s1, v255, 11
	s_cmp_lt_i32 s50, s1
	s_cselect_b64 s[2:3], -1, 0
	s_and_b64 s[0:1], s[6:7], s[2:3]
	s_andn2_b64 vcc, exec, s[0:1]
	s_cbranch_vccnz .LBB0_3857
	s_mov_b64 s[4:5], 0
	v_readlane_b32 s0, v255, 7
	s_waitcnt vmcnt(0)
	s_waitcnt vmcnt(0) lgkmcnt(0)
	s_barrier
	v_writelane_b32 v255, s0, 7
	s_mov_b64 s[0:1], exec
	v_readlane_b32 s6, v255, 8
	v_readlane_b32 s7, v255, 9
	s_and_b64 s[6:7], s[0:1], s[6:7]
	s_mov_b64 exec, s[6:7]
	s_cbranch_execz .LBB0_3856
	v_readlane_b32 s6, v255, 15
	s_waitcnt vmcnt(0) expcnt(0) lgkmcnt(0)
	buffer_inv sc0 sc1
	v_readlane_b32 s8, v255, 3
	v_mov_b32_e32 v0, s6
	ds_read_b32 v4, v0
	v_readlane_b32 s6, v255, 16
	v_readlane_b32 s10, v255, 5
	v_readlane_b32 s11, v255, 6
	v_mov_b32_e32 v0, s6
	ds_read_b32 v2, v0
	s_add_u32 s4, s10, s4
	s_waitcnt lgkmcnt(1)
	v_cmp_ne_u32_e32 vcc, 0, v4
	s_addc_u32 s5, s11, s5
	v_readlane_b32 s9, v255, 4
	s_cbranch_vccnz .LBB0_3820
	v_readlane_b32 s6, v255, 0
	v_readlane_b32 s7, v255, 1
	s_load_dwordx2 s[10:11], s[6:7], 0x4
	s_add_u32 s6, s4, 0x4200
	s_addc_u32 s7, s5, 0
	s_add_u32 s8, s4, 0x4400
	s_addc_u32 s9, s5, 0
	v_readlane_b32 s12, v255, 2
	s_waitcnt lgkmcnt(0)
	s_mul_i32 s51, s10, s12
	s_add_u32 s10, s4, 0x4500
	s_mul_i32 s51, s51, s11
	s_addc_u32 s11, s5, 0
	s_add_u32 s12, s4, 0x4600
	s_addc_u32 s13, s5, 0
	s_add_u32 s14, s4, 0x4700
	s_addc_u32 s15, s5, 0
	s_add_u32 s16, s4, 0x4800
	s_addc_u32 s17, s5, 0
	s_add_u32 s18, s4, 0x4900
	s_addc_u32 s19, s5, 0
	s_add_u32 s20, s4, 0x4a00
	s_addc_u32 s21, s5, 0
	s_add_u32 s22, s4, 0x4b00
	s_addc_u32 s23, s5, 0
	s_add_u32 s24, s4, 0x4c00
	s_addc_u32 s25, s5, 0
	s_add_u32 s26, s4, 0x4d00
	s_addc_u32 s27, s5, 0
	s_add_u32 s28, s4, 0x4e00
	s_addc_u32 s29, s5, 0
	s_add_u32 s30, s4, 0x4f00
	s_addc_u32 s31, s5, 0
	s_add_u32 s34, s4, 0x5000
	s_addc_u32 s35, s5, 0
	s_add_u32 s36, s4, 0x5100
	s_addc_u32 s37, s5, 0
	s_add_u32 s38, s4, 0x5200
	s_addc_u32 s39, s5, 0
	s_add_u32 s40, s4, 0x5300
	s_addc_u32 s41, s5, 0
	s_mov_b32 s52, 1
	s_branch .LBB0_3808

; __device__ __forceinline__ unsigned xb_ld(unsigned* p)              { return __hip_atomic_load(p, __ATOMIC_RELAXED, __HIP_MEMORY_SCOPE_AGENT); }
; #define XB_SPIN(cond, bar) do { unsigned _sp = 0; while (cond) { __builtin_amdgcn_s_sleep(1); \
;     if ((++_sp & 255u) == 0u) { if (xb_ld(&(bar)[XB_TMO])) break; if (_sp > XB_SPIN_CAP) { atomicAdd(&(bar)[XB_TMO], 1u); break; } } } } while (0)
; __device__ __forceinline__ void xcd_barrier(const XcdBarrier& b) {
;     ...
;             XB_SPIN(xb_ld(&bar[XB_XGEN(b.x)]) == gen, bar);
;             __builtin_amdgcn_fence(__ATOMIC_ACQUIRE, XB_SCOPE);
;             asm volatile("s_waitcnt vmcnt(0)" ::: "memory");
;         }
.Lmy_nl_B10:
	s_nop 0
.Lmy_nl2_B10:
	s_waitcnt vmcnt(0)

; __device__ __forceinline__ unsigned xb_add(unsigned* p, unsigned v) { return __hip_atomic_fetch_add(p, v, __ATOMIC_RELAXED, __HIP_MEMORY_SCOPE_AGENT); }
; __device__ __forceinline__ void xcd_barrier(const XcdBarrier& b) {
;     ...
;     if (threadIdx.x == 0) {
;         unsigned* bar = b.bar;
;         __builtin_amdgcn_s_waitcnt(0);
;         unsigned nloc = b.st[0], nx = b.st[1];
;         if (nloc == 0u) { xcd_barrier_complete(bar, b.x, nloc, nx); b.st[0] = nloc; b.st[1] = nx; }
;         const unsigned old = xb_add(&bar[XB_XSUB(b.x)], 1u);
.LBB0_3880:
	v_readlane_b32 s4, v255, 15
	s_waitcnt vmcnt(0) expcnt(0) lgkmcnt(0)
	buffer_inv sc0 sc1
	s_nop 0
	v_mov_b32_e32 v0, s4
	v_readlane_b32 s4, v255, 3
	ds_read_b32 v4, v0
	v_readlane_b32 s4, v255, 16
	v_readlane_b32 s6, v255, 5
	v_readlane_b32 s7, v255, 6
	v_mov_b32_e32 v0, s4
	ds_read_b32 v2, v0
	s_add_u32 s2, s6, s2
	s_waitcnt lgkmcnt(1)
	v_cmp_ne_u32_e32 vcc, 0, v4
	s_addc_u32 s3, s7, s3
	v_readlane_b32 s5, v255, 4
	s_cbranch_vccnz .LBB0_3895
	v_readlane_b32 s4, v255, 0
	v_readlane_b32 s5, v255, 1
	s_load_dwordx2 s[8:9], s[4:5], 0x4
	s_add_u32 s4, s2, 0x4200
	s_addc_u32 s5, s3, 0
	s_add_u32 s6, s2, 0x4400
	s_addc_u32 s7, s3, 0
	v_readlane_b32 s10, v255, 2
	s_waitcnt lgkmcnt(0)
	s_mul_i32 s46, s8, s10
	s_add_u32 s8, s2, 0x4500
	s_mul_i32 s46, s46, s9
	s_addc_u32 s9, s3, 0
	s_add_u32 s10, s2, 0x4600
	s_addc_u32 s11, s3, 0
	s_add_u32 s12, s2, 0x4700
	s_addc_u32 s13, s3, 0
	s_add_u32 s14, s2, 0x4800
	s_addc_u32 s15, s3, 0
	s_add_u32 s16, s2, 0x4900
	s_addc_u32 s17, s3, 0
	s_add_u32 s18, s2, 0x4a00
	s_addc_u32 s19, s3, 0
	s_add_u32 s20, s2, 0x4b00
	s_addc_u32 s21, s3, 0
	s_add_u32 s22, s2, 0x4c00
	s_addc_u32 s23, s3, 0
	s_add_u32 s24, s2, 0x4d00
	s_addc_u32 s25, s3, 0
	s_add_u32 s26, s2, 0x4e00
	s_addc_u32 s27, s3, 0
	s_add_u32 s28, s2, 0x4f00
	s_addc_u32 s29, s3, 0
	s_add_u32 s30, s2, 0x5000
	s_addc_u32 s31, s3, 0
	s_add_u32 s34, s2, 0x5100
	s_addc_u32 s35, s3, 0
	s_add_u32 s36, s2, 0x5200
	s_addc_u32 s37, s3, 0
	s_add_u32 s38, s2, 0x5300
	s_addc_u32 s39, s3, 0
	s_mov_b32 s47, 1
	s_branch .LBB0_3883

; __device__ __forceinline__ unsigned xb_ld(unsigned* p)              { return __hip_atomic_load(p, __ATOMIC_RELAXED, __HIP_MEMORY_SCOPE_AGENT); }
; #define XB_SPIN(cond, bar) do { unsigned _sp = 0; while (cond) { __builtin_amdgcn_s_sleep(1); \
;     if ((++_sp & 255u) == 0u) { if (xb_ld(&(bar)[XB_TMO])) break; if (_sp > XB_SPIN_CAP) { atomicAdd(&(bar)[XB_TMO], 1u); break; } } } } while (0)
; __device__ __forceinline__ void xcd_barrier(const XcdBarrier& b) {
;     ...
;             XB_SPIN(xb_ld(&bar[XB_XGEN(b.x)]) == gen, bar);
;             __builtin_amdgcn_fence(__ATOMIC_ACQUIRE, XB_SCOPE);
;             asm volatile("s_waitcnt vmcnt(0)" ::: "memory");
;         }
.LBB0_3910:
	s_or_b64 exec, exec, s[6:7]
	s_waitcnt vmcnt(0) lgkmcnt(0)
	s_nop 0
	s_waitcnt vmcnt(0)

; __device__ __forceinline__ unsigned xb_ld(unsigned* p)              { return __hip_atomic_load(p, __ATOMIC_RELAXED, __HIP_MEMORY_SCOPE_AGENT); }
; __device__ __forceinline__ unsigned xb_add(unsigned* p, unsigned v) { return __hip_atomic_fetch_add(p, v, __ATOMIC_RELAXED, __HIP_MEMORY_SCOPE_AGENT); }
; #define XB_SPIN(cond, bar) do { unsigned _sp = 0; while (cond) { __builtin_amdgcn_s_sleep(1); \
;     if ((++_sp & 255u) == 0u) { if (xb_ld(&(bar)[XB_TMO])) break; if (_sp > XB_SPIN_CAP) { atomicAdd(&(bar)[XB_TMO], 1u); break; } } } } while (0)
; __device__ __forceinline__ void xcd_barrier(const XcdBarrier& b) {
;     ...
;             else XB_SPIN(xb_ld(&bar[XB_TOPGEN]) == tg, bar);
;             __builtin_amdgcn_fence(__ATOMIC_ACQUIRE, XB_SCOPE);
;             xb_add(&bar[XB_XGEN(b.x)], 1u);
;             asm volatile("s_waitcnt vmcnt(0)" ::: "memory");
.LBB0_3928:
	s_or_b64 exec, exec, s[2:3]
	s_mov_b64 s[2:3], exec
	v_mbcnt_lo_u32_b32 v0, s2, 0
	v_mbcnt_hi_u32_b32 v0, s3, v0
	v_cmp_eq_u32_e32 vcc, 0, v0
	s_waitcnt vmcnt(0)
	s_nop 0
	s_and_saveexec_b64 s[4:5], vcc
	s_cbranch_execnz .LBB0_3929
	s_getpc_b64 s[98:99]
